# attention softmax: exp2((s-m)*log2e) folded into one fma per score (on top of the bonus-scalar handoff P4a->P5)
# speedup vs baseline: 1.0081x; 1.0039x over previous
; __device__ __forceinline__ unsigned cvt_pk_bf16(float lo, float hi) { const f32x2_t_ v = {lo, hi}; const bf16x2_t_ b = __builtin_convertvector(v, bf16x2_t_); return __builtin_bit_cast(unsigned, b); }
; __device__ __forceinline__ void p2_shift_attn(Frame& F0, const In& I) {
;     ...
;                 { const unsigned mu_ = __builtin_bit_cast(unsigned, mx);
;                   const auto sw_ = __builtin_amdgcn_permlane32_swap(mu_, mu_, false, false);
;                   mx = fmaxf(__builtin_bit_cast(float, sw_[0]), __builtin_bit_cast(float, sw_[1])); }
;                 const float m_new = fmaxf(m_run, mx), alpha = __expf(m_run - m_new);
;                 float ls = 0.f;
; #pragma unroll
;                 for (int tt = 0; tt < 2; ++tt)
; #pragma unroll
;                     for (int i = 0; i < 16; ++i) { st[tt][i] = __expf(st[tt][i] - m_new); ls += st[tt][i]; }
;                 l_run = l_run * alpha + ls;
;                 if (__builtin_amdgcn_ballot_w64(m_new != m_run)) {
; #pragma unroll
;                     for (int i = 0; i < 16; ++i) { o0[i] *= alpha; o1[i] *= alpha; } }
;                 m_run = m_new;
; #pragma unroll
;                 for (int tt = 0; tt < 2; ++tt)
; #pragma unroll
;                     for (int s2 = 0; s2 < 2; ++s2) {
;                         v4u pw; pw.x = pg8::cvt_pk_bf16(st[tt][8 * s2 + 0], st[tt][8 * s2 + 1]); pw.y = pg8::cvt_pk_bf16(st[tt][8 * s2 + 2], st[tt][8 * s2 + 3]); pw.z = pg8::cvt_pk_bf16(st[tt][8 * s2 + 4], st[tt][8 * s2 + 5]); pw.w = pg8::cvt_pk_bf16(st[tt][8 * s2 + 6], st[tt][8 * s2 + 7]);
;                         const bf16x8 pf = __builtin_bit_cast(bf16x8, pw);
;                         o0 = __builtin_amdgcn_mfma_f32_32x32x16_bf16(va[tt][s2], pf, o0, 0, 0, 0);
;                         o1 = __builtin_amdgcn_mfma_f32_32x32x16_bf16(vb[tt][s2], pf, o1, 0, 0, 0);
;                     }
.LBB0_895:
	v_mov_b32_e32 v3, v171
	s_nop 1
	v_permlane32_swap_b32_e32 v171, v3
	v_max_f32_e32 v3, v169, v169
	v_max_f32_e32 v36, v171, v171
	v_max_f32_e32 v3, v3, v36
	s_mov_b32 s98, 0x3fb8aa3b
	s_mov_b32 s99, 0xbfb8aa3b
	v_mul_f32_e32 v176, s99, v3
	v_sub_f32_e32 v36, v169, v3
	v_mul_f32_e32 v36, 0x3fb8aa3b, v36
	v_exp_f32_e32 v36, v36
	v_cmp_neq_f32_e32 vcc, v3, v169
	s_cbranch_vccz .LBB0_897
	v_pk_mul_f32 v[34:35], v[34:35], v[36:37] op_sel_hi:[1,0]
	v_pk_mul_f32 v[32:33], v[32:33], v[36:37] op_sel_hi:[1,0]
	v_pk_mul_f32 v[30:31], v[30:31], v[36:37] op_sel_hi:[1,0]
	v_pk_mul_f32 v[28:29], v[28:29], v[36:37] op_sel_hi:[1,0]
	v_pk_mul_f32 v[26:27], v[26:27], v[36:37] op_sel_hi:[1,0]
	v_pk_mul_f32 v[24:25], v[24:25], v[36:37] op_sel_hi:[1,0]
	v_pk_mul_f32 v[22:23], v[22:23], v[36:37] op_sel_hi:[1,0]
	v_pk_mul_f32 v[20:21], v[20:21], v[36:37] op_sel_hi:[1,0]
	v_pk_mul_f32 v[18:19], v[18:19], v[36:37] op_sel_hi:[1,0]
	v_pk_mul_f32 v[16:17], v[16:17], v[36:37] op_sel_hi:[1,0]
	v_pk_mul_f32 v[14:15], v[14:15], v[36:37] op_sel_hi:[1,0]
	v_pk_mul_f32 v[12:13], v[12:13], v[36:37] op_sel_hi:[1,0]
	v_pk_mul_f32 v[10:11], v[10:11], v[36:37] op_sel_hi:[1,0]
	v_pk_mul_f32 v[8:9], v[8:9], v[36:37] op_sel_hi:[1,0]
	v_pk_mul_f32 v[6:7], v[6:7], v[36:37] op_sel_hi:[1,0]
	v_pk_mul_f32 v[4:5], v[4:5], v[36:37] op_sel_hi:[1,0]
.LBB0_897:
	v_fma_f32 v37, v152, s98, v176
	v_fma_f32 v38, v153, s98, v176
	v_exp_f32_e32 v37, v37
	v_fma_f32 v39, v150, s98, v176
	v_exp_f32_e32 v38, v38
	v_fma_f32 v40, v151, s98, v176
	v_exp_f32_e32 v39, v39
	v_fma_f32 v42, v146, s98, v176
	v_exp_f32_e32 v40, v40
	v_fma_f32 v43, v147, s98, v176
	v_add_f32_e32 v41, 0, v37
	v_exp_f32_e32 v42, v42
	v_fma_f32 v44, v148, s98, v176
	v_add_f32_e32 v41, v38, v41
	v_exp_f32_e32 v43, v43
	v_fma_f32 v45, v149, s98, v176
	v_add_f32_e32 v41, v39, v41
	v_exp_f32_e32 v44, v44
	v_fma_f32 v46, v158, s98, v176
	v_add_f32_e32 v41, v40, v41
	v_exp_f32_e32 v45, v45
	v_fma_f32 v47, v159, s98, v176
	v_add_f32_e32 v41, v42, v41
	v_exp_f32_e32 v46, v46
	v_fma_f32 v48, v160, s98, v176
	v_add_f32_e32 v41, v43, v41
	v_exp_f32_e32 v47, v47
	v_fma_f32 v49, v161, s98, v176
	v_add_f32_e32 v41, v44, v41
	v_exp_f32_e32 v48, v48
	v_fma_f32 v50, v154, s98, v176
	v_add_f32_e32 v41, v45, v41
	v_exp_f32_e32 v49, v49
	v_fma_f32 v51, v155, s98, v176
	v_add_f32_e32 v41, v46, v41
	v_exp_f32_e32 v50, v50
	v_fma_f32 v146, v156, s98, v176
	v_add_f32_e32 v41, v47, v41
	v_exp_f32_e32 v51, v51
	v_fma_f32 v147, v157, s98, v176
	v_add_f32_e32 v41, v48, v41
	v_exp_f32_e32 v146, v146
	v_fma_f32 v62, v62, s98, v176
	v_add_f32_e32 v41, v49, v41
	v_exp_f32_e32 v147, v147
	v_fma_f32 v63, v63, s98, v176
	v_add_f32_e32 v41, v50, v41
	v_exp_f32_e32 v62, v62
	v_fma_f32 v60, v60, s98, v176
	v_add_f32_e32 v41, v51, v41
	v_exp_f32_e32 v63, v63
	v_fma_f32 v61, v61, s98, v176
	v_add_f32_e32 v41, v146, v41
	v_exp_f32_e32 v60, v60
	v_add_f32_e32 v41, v147, v41
	v_exp_f32_e32 v61, v61
	v_add_f32_e32 v41, v62, v41
	v_add_f32_e32 v41, v63, v41
	v_add_f32_e32 v41, v60, v41
	v_add_f32_e32 v148, v61, v41
	v_fma_f32 v41, v56, s98, v176
	v_exp_f32_e32 v56, v41
	v_fma_f32 v41, v57, s98, v176
	v_exp_f32_e32 v57, v41
	v_fma_f32 v41, v58, s98, v176
	v_exp_f32_e32 v58, v41
	v_fma_f32 v41, v59, s98, v176
	v_exp_f32_e32 v59, v41
	v_cvt_pk_bf16_f32 v38, v37, v38
	v_cvt_pk_bf16_f32 v39, v39, v40
	v_cvt_pk_bf16_f32 v40, v42, v43
	v_cvt_pk_bf16_f32 v41, v44, v45
	v_fma_f32 v42, v66, s98, v176
	s_waitcnt lgkmcnt(7)
	v_mfma_f32_32x32x16_bf16 v[20:35], v[120:123], v[38:41], v[20:35]
	v_fma_f32 v44, v64, s98, v176
	v_fma_f32 v45, v65, s98, v176
	v_add_f32_e32 v37, v56, v148
	v_exp_f32_e32 v42, v42
	v_add_f32_e32 v37, v57, v37
	s_waitcnt lgkmcnt(5)
	v_mfma_f32_32x32x16_bf16 v[4:19], v[116:119], v[38:41], v[4:19]
	v_fma_f32 v38, v67, s98, v176
	v_exp_f32_e32 v43, v38
	v_cvt_pk_bf16_f32 v38, v46, v47
	v_cvt_pk_bf16_f32 v39, v48, v49
	v_cvt_pk_bf16_f32 v40, v50, v51
	v_cvt_pk_bf16_f32 v41, v146, v147
	v_fma_f32 v47, v53, s98, v176
	v_fma_f32 v48, v54, s98, v176
	v_mfma_f32_32x32x16_bf16 v[20:35], v[112:115], v[38:41], v[20:35]
	v_exp_f32_e32 v44, v44
	v_exp_f32_e32 v45, v45
	v_exp_f32_e32 v47, v47
	v_exp_f32_e32 v48, v48
	v_add_f32_e32 v37, v58, v37
	s_waitcnt lgkmcnt(4)
	v_mfma_f32_32x32x16_bf16 v[4:19], v[108:111], v[38:41], v[4:19]
	v_fma_f32 v46, v52, s98, v176
	v_cvt_pk_bf16_f32 v38, v62, v63
	v_cvt_pk_bf16_f32 v39, v60, v61
	v_cvt_pk_bf16_f32 v40, v56, v57
	v_cvt_pk_bf16_f32 v41, v58, v59
	v_exp_f32_e32 v46, v46
	v_add_f32_e32 v37, v59, v37
	s_waitcnt lgkmcnt(3)
	v_mfma_f32_32x32x16_bf16 v[20:35], v[104:107], v[38:41], v[20:35]
	v_add_f32_e32 v37, v42, v37
	v_add_f32_e32 v37, v43, v37
	v_add_f32_e32 v37, v44, v37
	v_add_f32_e32 v37, v45, v37
	v_add_f32_e32 v37, v46, v37
	v_add_f32_e32 v37, v47, v37
	v_add_f32_e32 v37, v48, v37
	s_waitcnt lgkmcnt(1)
	v_mfma_f32_32x32x16_bf16 v[4:19], v[100:103], v[38:41], v[4:19]
	v_fma_f32 v38, v55, s98, v176
	v_exp_f32_e32 v49, v38
	v_cvt_pk_bf16_f32 v38, v42, v43
	v_cvt_pk_bf16_f32 v39, v44, v45
	v_cvt_pk_bf16_f32 v40, v46, v47
	v_cvt_pk_bf16_f32 v41, v48, v49
	v_add_f32_e32 v37, v49, v37
	v_fmac_f32_e32 v37, v168, v36
	v_mfma_f32_32x32x16_bf16 v[20:35], v[96:99], v[38:41], v[20:35]
	v_mov_b32_e32 v168, v37
	s_waitcnt lgkmcnt(0)
	v_mfma_f32_32x32x16_bf16 v[4:19], v[92:95], v[38:41], v[4:19]
	s_andn2_b64 vcc, exec, s[16:17]
	s_cbranch_vccz .LBB0_886
	s_branch .LBB0_887
